# in-projection GEMM to chunk-local mixer pass handoff made quad-local (conv halo rows passed through a write-through side buffer); 6 grid barriers removed in total
# speedup vs baseline: 1.0039x; 1.0039x over previous
.LBB0_194:
	s_add_u32 s0, s18, 0x4400
	s_addc_u32 s1, s19, 0
	v_mbcnt_hi_u32_b32 v0, -1, v217
	v_lshlrev_b32_e32 v1, 8, v0
	v_and_b32_e32 v1, 0x700, v1
	global_load_dword v2, v1, s[0:1] sc1
	v_mov_b32_e32 v3, 0x24a70
	ds_read_b32 v3, v3
	s_waitcnt vmcnt(0) lgkmcnt(0)
	s_getreg_b32 s0, hwreg(HW_REG_XCC_ID, 0, 4)
	v_cmp_eq_u32_e32 vcc, 32, v2
	s_nop 1
	s_cmp_eq_u64 vcc, exec
	s_cselect_b32 s100, 1, 0
	s_cmp_eq_u32 s38, 0x100
	s_cselect_b32 s100, s100, 0
	v_readfirstlane_b32 s1, v3
	s_nop 3
	s_lshl_b32 s98, s0, 3
	s_lshr_b32 s0, s1, 2
	s_add_i32 s98, s98, s0
	s_and_b32 s99, s1, 3
	s_lshr_b32 s0, s99, 1
	s_lshl_b32 s101, s98, 1
	s_add_i32 s101, s101, s0
	s_cmp_lt_i32 s90, 2
	s_cselect_b64 s[0:1], -1, 0
	s_and_b64 s[4:5], s[0:1], s[2:3]
	s_andn2_b64 vcc, exec, s[4:5]
	s_cbranch_vccnz .LBB0_211
	s_and_b32 s0, s80, 0xffffffc0
	v_mbcnt_hi_u32_b32 v132, -1, v217
	v_add_u32_e32 v0, s0, v132
	v_mov_b32_e32 v1, v0
	s_mov_b64 s[0:1], s[86:87]
	s_mov_b64 s[2:3], s[18:19]
	s_cmpk_gt_i32 s6, 0x2ff
	s_cbranch_scc1 .LBB0_211
	v_bfe_i32 v3, v0, 27, 1
	v_lshlrev_b32_e32 v1, 4, v0
	v_lshrrev_b32_e32 v3, 22, v3
	v_add_u32_e32 v3, v1, v3
	v_and_b32_e32 v3, 0xfffffc00, v3
	v_sub_u32_e32 v3, v1, v3
	v_ashrrev_i32_e32 v2, 31, v0
	v_lshrrev_b32_e32 v4, 4, v3
	v_lshrrev_b32_e32 v2, 26, v2
	v_bitop3_b32 v3, v4, v3, 32 bitop3:0x6c
	s_waitcnt lgkmcnt(0)
	s_add_u32 s8, s2, 0x12400000
	v_add_u32_e32 v2, v0, v2
	v_ashrrev_i32_e32 v5, 31, v3
	s_addc_u32 s0, s3, 0
	v_ashrrev_i32_e32 v2, 6, v2
	v_lshrrev_b32_e32 v5, 26, v5
	s_add_u32 s12, s2, 0xc00000
	v_lshlrev_b32_e32 v4, 3, v2
	v_add_u32_e32 v5, v3, v5
	s_addc_u32 s1, s3, 0
	v_and_b32_e32 v4, -16, v4
	v_ashrrev_i32_e32 v6, 6, v5
	v_and_b32_e32 v5, 0xc0, v5
	s_and_b32 s9, s0, 0xffff
	s_ashr_i32 s0, s6, 31
	v_add_u32_e32 v4, v6, v4
	v_sub_u32_e32 v3, v3, v5
	v_mov_b32_e32 v5, 1
	s_and_b32 s13, s1, 0xffff
	s_lshr_b32 s1, s0, 29
	v_lshlrev_b32_e32 v2, 5, v2
	v_ashrrev_i16_sdwa v3, v5, sext(v3) dst_sel:DWORD dst_unused:UNUSED_PAD src0_sel:DWORD src1_sel:BYTE_0
	v_lshlrev_b32_e32 v7, 1, v4
	v_lshlrev_b32_e32 v8, 2, v4
	v_lshrrev_b32_e32 v9, 2, v4
	v_and_b32_e32 v6, 3, v6
	s_add_i32 s1, s6, s1
	v_and_b32_e32 v2, 32, v2
	v_bfe_i32 v3, v3, 0, 16
	v_and_b32_e32 v7, 0x1fffc0, v7
	v_and_b32_e32 v9, 4, v9
	v_and_or_b32 v6, v8, 48, v6
	s_ashr_i32 s20, s1, 3
	s_and_b32 s1, s1, -8
	v_or3_b32 v6, v6, v7, v9
	v_add_lshl_u32 v2, v2, v3, 1
	v_add_u32_e32 v1, 0x2000, v1
	s_lshr_b32 s24, s80, 8
	s_lshl_b32 s7, s88, 10
	s_sub_i32 s21, s6, s1
	v_lshl_add_u32 v133, v4, 11, v2
	v_lshl_add_u32 v134, v6, 11, v2
	v_ashrrev_i32_e32 v2, 31, v1
	s_cmp_lt_i32 s21, 0
	s_movk_i32 s1, 0x61
	v_lshrrev_b32_e32 v2, 22, v2
	s_cselect_b32 s22, s1, 0x60
	v_add_u32_e32 v2, v1, v2
	s_mul_i32 s21, s21, s22
	v_ashrrev_i32_e32 v2, 10, v2
	s_add_i32 s21, s21, s20
	v_mul_i32_i24_e32 v3, 0x400, v2
	s_mul_hi_i32 s20, s21, 0x2aaaaaab
	v_sub_u32_e32 v1, v1, v3
	s_lshr_b32 s22, s20, 31
	s_ashr_i32 s20, s20, 3
	v_lshrrev_b32_e32 v3, 4, v1
	s_add_i32 s20, s20, s22
	v_bitop3_b32 v1, v3, v1, 32 bitop3:0x6c
	s_lshl_b32 s22, s20, 3
	s_mul_i32 s20, s20, 48
	v_ashrrev_i32_e32 v4, 31, v1
	s_sub_i32 s20, s21, s20
	v_lshrrev_b32_e32 v4, 26, v4
	s_bfe_i32 s21, s20, 0x80000
	v_lshlrev_b32_e32 v3, 3, v2
	v_add_u32_e32 v4, v1, v4
	s_bfe_u32 s21, s21, 0x3000c
	v_and_b32_e32 v3, -16, v3
	v_ashrrev_i32_e32 v6, 6, v4
	v_and_b32_e32 v4, 0xc0, v4
	s_add_i32 s21, s20, s21
	v_add_u32_e32 v3, v6, v3
	v_sub_u32_e32 v1, v1, v4
	s_bfe_i32 s23, s21, 0x80000
	v_lshlrev_b32_e32 v2, 5, v2
	v_ashrrev_i16_sdwa v1, v5, sext(v1) dst_sel:DWORD dst_unused:UNUSED_PAD src0_sel:DWORD src1_sel:BYTE_0
	v_lshlrev_b32_e32 v4, 1, v3
	v_lshlrev_b32_e32 v5, 2, v3
	v_lshrrev_b32_e32 v7, 2, v3
	v_and_b32_e32 v6, 3, v6
	s_sext_i32_i16 s23, s23
	s_add_i32 s7, s7, 0
	v_and_b32_e32 v2, 32, v2
	v_bfe_i32 v1, v1, 0, 16
	v_and_b32_e32 v4, 0x1fffc0, v4
	v_and_b32_e32 v7, 4, v7
	v_and_or_b32 v5, v5, 48, v6
	s_mov_b32 s11, 0x20000
	s_brev_b32 s10, -2
	s_and_b32 s21, s21, 0xf8
	s_ashr_i32 s54, s23, 3
	s_cmp_eq_u32 s100, 1
	s_cbranch_scc0 .Lqo_p1i1
	s_mov_b32 s54, s99
.Lqo_p1i1:
	s_add_i32 s26, s7, 0x10000
	v_or3_b32 v4, v5, v4, v7
	v_add_lshl_u32 v1, v2, v1, 1
	s_mov_b32 s14, s10
	s_mov_b32 s15, s11
	s_sub_i32 s20, s20, s21
	s_lshl_b32 s56, s54, 19
	s_mov_b32 m0, s26
	s_add_i32 s27, s7, 0x12000
	v_lshl_add_u32 v136, v4, 11, v1
	s_sext_i32_i8 s20, s20
	buffer_load_dwordx4 v134, s[12:15], s56 offen lds
	s_mov_b32 m0, s27
	s_add_i32 s28, s7, 0x14000
	s_add_i32 s55, s22, s20
	s_cmp_eq_u32 s100, 1
	s_cbranch_scc0 .Lqo_p1i2
	s_lshl_b32 s55, s98, 1
.Lqo_p1i2:
	buffer_load_dwordx4 v136, s[12:15], s56 offen lds
	s_or_b32 s20, s56, 0x4000
	s_mov_b32 m0, s28
	s_add_i32 s29, s7, 0x16000
	buffer_load_dwordx4 v134, s[12:15], s20 offen lds
	s_mov_b32 m0, s29
	s_lshl_b32 s57, s55, 19
	buffer_load_dwordx4 v136, s[12:15], s20 offen lds
	s_mov_b32 m0, s7
	s_add_i32 s30, s7, 0x2000
	v_lshl_add_u32 v135, v3, 11, v1
	buffer_load_dwordx4 v133, s[8:11], s57 offen lds
	s_mov_b32 m0, s30
	s_add_i32 s31, s7, 0x4000
	buffer_load_dwordx4 v135, s[8:11], s57 offen lds
	s_or_b32 s14, s57, 0x40000
	s_mov_b32 m0, s31
	s_add_i32 s33, s7, 0x6000
	buffer_load_dwordx4 v133, s[8:11], s14 offen lds
	s_mov_b32 m0, s33
	s_cmp_eq_u32 s24, 1
	buffer_load_dwordx4 v135, s[8:11], s14 offen lds
	s_cselect_b64 s[20:21], -1, 0
	s_cmp_lg_u32 s24, 1
	s_cbranch_scc1 .LBB0_198
	s_barrier

.LBB0_203:
	s_cmp_eq_u32 s100, 1
	s_cbranch_scc0 .Lqo_p1n
	s_lshl_b32 s50, s44, 2
	s_add_i32 s50, s50, s99
	s_cmp_ge_u32 s50, 6
	s_cselect_b32 s51, 1, 0
	s_cselect_b32 s14, 6, 0
	s_sub_i32 s50, s50, s14
	s_lshl_b32 s15, s98, 1
	s_add_i32 s51, s51, s15

.LBB0_207:
	s_lshl_b32 s14, s55, 8
	v_mov_b32_e32 v139, v132
	s_add_i32 s14, s14, s43
	v_cvt_pk_bf16_f32 v104, v104, v105
	v_and_or_b32 v144, v139, 15, s14
	s_lshl_b32 s14, s54, 8
	s_or_b32 s14, s14, s46
	v_and_b32_e32 v139, -16, v139
	v_add_u32_e32 v140, s14, v139
	v_ashrrev_i32_e32 v141, 31, v140
	v_lshl_add_u64 v[140:141], v[140:141], 1, s[22:23]
	v_mad_i64_i32 v[142:143], s[14:15], v144, s49, v[140:141]
	v_cvt_pk_bf16_f32 v105, v106, v107
	v_cvt_pk_bf16_f32 v106, v112, v113
	v_cvt_pk_bf16_f32 v107, v114, v115
	global_store_dwordx4 v[142:143], v[104:107], off
	v_cvt_pk_bf16_f32 v80, v80, v81
	v_cvt_pk_bf16_f32 v81, v82, v83
	v_cvt_pk_bf16_f32 v104, v120, v121
	v_cvt_pk_bf16_f32 v105, v122, v123
	v_cvt_pk_bf16_f32 v106, v124, v125
	v_cvt_pk_bf16_f32 v107, v126, v127
	global_store_dwordx4 v[142:143], v[104:107], off offset:16
	v_cvt_pk_bf16_f32 v82, v88, v89
	v_cvt_pk_bf16_f32 v83, v90, v91
	v_or_b32_e32 v104, 16, v144
	v_mad_i64_i32 v[104:105], s[14:15], v104, s49, v[140:141]
	global_store_dwordx4 v[104:105], v[80:83], off
	v_cvt_pk_bf16_f32 v40, v40, v41
	v_cvt_pk_bf16_f32 v41, v42, v43
	v_cvt_pk_bf16_f32 v80, v108, v109
	v_cvt_pk_bf16_f32 v81, v110, v111
	v_cvt_pk_bf16_f32 v82, v116, v117
	v_cvt_pk_bf16_f32 v83, v118, v119
	global_store_dwordx4 v[104:105], v[80:83], off offset:16
	v_cvt_pk_bf16_f32 v42, v52, v53
	v_cvt_pk_bf16_f32 v43, v54, v55
	v_or_b32_e32 v80, 32, v144
	v_mad_i64_i32 v[80:81], s[14:15], v80, s49, v[140:141]
	global_store_dwordx4 v[80:81], v[40:43], off
	v_cvt_pk_bf16_f32 v20, v20, v21
	v_cvt_pk_bf16_f32 v21, v22, v23
	v_cvt_pk_bf16_f32 v40, v84, v85
	v_cvt_pk_bf16_f32 v41, v86, v87
	v_cvt_pk_bf16_f32 v42, v96, v97
	v_cvt_pk_bf16_f32 v43, v98, v99
	global_store_dwordx4 v[80:81], v[40:43], off offset:16
	v_cvt_pk_bf16_f32 v22, v32, v33
	v_cvt_pk_bf16_f32 v23, v34, v35
	v_or_b32_e32 v40, 48, v144
	v_mad_i64_i32 v[40:41], s[14:15], v40, s49, v[140:141]
	global_store_dwordx4 v[40:41], v[20:23], off
	v_cvt_pk_bf16_f32 v8, v8, v9
	v_cvt_pk_bf16_f32 v9, v10, v11
	v_cvt_pk_bf16_f32 v20, v64, v65
	v_cvt_pk_bf16_f32 v21, v66, v67
	v_cvt_pk_bf16_f32 v22, v72, v73
	v_cvt_pk_bf16_f32 v23, v74, v75
	global_store_dwordx4 v[40:41], v[20:23], off offset:16
	v_cvt_pk_bf16_f32 v10, v12, v13
	v_cvt_pk_bf16_f32 v11, v14, v15
	v_add_u32_e32 v20, 0x80, v144
	v_mad_i64_i32 v[32:33], s[14:15], v20, s49, v[140:141]
	v_cvt_pk_bf16_f32 v20, v48, v49
	v_cvt_pk_bf16_f32 v21, v50, v51
	v_cvt_pk_bf16_f32 v22, v60, v61
	v_cvt_pk_bf16_f32 v23, v62, v63
	global_store_dwordx4 v[32:33], v[20:23], off
	v_cvt_pk_bf16_f32 v0, v0, v1
	v_cvt_pk_bf16_f32 v1, v2, v3
	v_cvt_pk_bf16_f32 v20, v92, v93
	v_cvt_pk_bf16_f32 v21, v94, v95
	v_cvt_pk_bf16_f32 v22, v100, v101
	v_cvt_pk_bf16_f32 v23, v102, v103
	global_store_dwordx4 v[32:33], v[20:23], off offset:16
	v_cvt_pk_bf16_f32 v2, v4, v5
	v_cvt_pk_bf16_f32 v3, v6, v7
	v_add_u32_e32 v20, 0x90, v144
	v_mad_i64_i32 v[32:33], s[14:15], v20, s49, v[140:141]
	v_cvt_pk_bf16_f32 v20, v28, v29
	v_cvt_pk_bf16_f32 v21, v30, v31
	v_cvt_pk_bf16_f32 v22, v36, v37
	v_cvt_pk_bf16_f32 v23, v38, v39
	global_store_dwordx4 v[32:33], v[20:23], off
	s_andn2_b64 vcc, exec, s[2:3]
	s_mov_b64 s[2:3], -1
	v_cvt_pk_bf16_f32 v20, v68, v69
	v_cvt_pk_bf16_f32 v21, v70, v71
	v_cvt_pk_bf16_f32 v22, v76, v77
	v_cvt_pk_bf16_f32 v23, v78, v79
	global_store_dwordx4 v[32:33], v[20:23], off offset:16
	s_nop 1
	v_add_u32_e32 v20, 0xa0, v144
	v_mad_i64_i32 v[20:21], s[14:15], v20, s49, v[140:141]
	global_store_dwordx4 v[20:21], v[8:11], off
	s_nop 1
	v_cvt_pk_bf16_f32 v8, v44, v45
	v_cvt_pk_bf16_f32 v9, v46, v47
	v_cvt_pk_bf16_f32 v10, v56, v57
	v_cvt_pk_bf16_f32 v11, v58, v59
	global_store_dwordx4 v[20:21], v[8:11], off offset:16
	s_nop 1
	v_add_u32_e32 v8, 0xb0, v144
	v_mad_i64_i32 v[8:9], s[14:15], v8, s49, v[140:141]
	global_store_dwordx4 v[8:9], v[0:3], off
	s_cmp_eq_u32 s100, 1
	s_cbranch_scc0 .Lh1_1
	s_cmpk_lt_u32 s80, 0x100
	s_cbranch_scc1 .Lh1_1
	s_and_b32 s72, s55, 1
	s_cmp_eq_u32 s72, 1
	s_cbranch_scc0 .Lh1_1
	s_sub_u32 s72, s54, 2
	s_cmp_lt_u32 s72, 2
	s_cbranch_scc0 .Lh1_1
	s_add_i32 s72, s55, 1
	s_lshr_b32 s72, s72, 1
	s_mul_i32 s72, s72, 1563648
	s_sub_u32 s70, 0xe002400, s72
	s_mov_b32 s71, 0
	v_and_b32_e32 v204, 15, v144
	v_cmp_lt_u32_e64 s[68:69], 12, v204
	s_nop 3
	s_and_saveexec_b64 s[66:67], s[68:69]
	v_lshl_add_u64 v[204:205], v[8:9], 0, s[70:71]
	global_store_dwordx4 v[204:205], v[0:3], off sc1
	s_mov_b64 exec, s[66:67]
.Lh1_1:
	s_nop 1
	v_cvt_pk_bf16_f32 v0, v24, v25
	v_cvt_pk_bf16_f32 v1, v26, v27
	v_cvt_pk_bf16_f32 v2, v16, v17
	v_cvt_pk_bf16_f32 v3, v18, v19
	global_store_dwordx4 v[8:9], v[0:3], off offset:16
	s_cmp_eq_u32 s100, 1
	s_cbranch_scc0 .Lh1_2
	s_cmpk_lt_u32 s80, 0x100
	s_cbranch_scc1 .Lh1_2
	s_and_b32 s72, s55, 1
	s_cmp_eq_u32 s72, 1
	s_cbranch_scc0 .Lh1_2
	s_sub_u32 s72, s54, 2
	s_cmp_lt_u32 s72, 2
	s_cbranch_scc0 .Lh1_2
	s_add_i32 s72, s55, 1
	s_lshr_b32 s72, s72, 1
	s_mul_i32 s72, s72, 1563648
	s_sub_u32 s70, 0xe002400, s72
	s_mov_b32 s71, 0
	v_and_b32_e32 v204, 15, v144
	v_cmp_lt_u32_e64 s[68:69], 12, v204
	s_nop 3
	s_and_saveexec_b64 s[66:67], s[68:69]
	v_lshl_add_u64 v[204:205], v[8:9], 0, s[70:71]
	global_store_dwordx4 v[204:205], v[0:3], off offset:16 sc1
	s_mov_b64 exec, s[66:67]
.Lh1_2:
	s_cbranch_vccnz .LBB0_200
	v_mov_b32_e32 v16, 0
	s_andn2_b64 vcc, exec, s[20:21]
	s_nop 0
	v_mfma_f32_4x4x1_16b_f32 v[104:107], v16, v16, 0
	s_nop 0
	v_mfma_f32_4x4x1_16b_f32 v[112:115], v16, v16, 0
	s_nop 0
	v_mfma_f32_4x4x1_16b_f32 v[80:83], v16, v16, 0
	s_nop 0
	v_mfma_f32_4x4x1_16b_f32 v[88:91], v16, v16, 0
	s_nop 0
	v_mfma_f32_4x4x1_16b_f32 v[40:43], v16, v16, 0
	s_nop 0
	v_mfma_f32_4x4x1_16b_f32 v[52:55], v16, v16, 0
	s_nop 0
	v_mfma_f32_4x4x1_16b_f32 v[20:23], v16, v16, 0
	s_nop 0
	v_mfma_f32_4x4x1_16b_f32 v[32:35], v16, v16, 0
	s_nop 0
	v_mfma_f32_4x4x1_16b_f32 v[120:123], v16, v16, 0
	s_nop 0
	v_mfma_f32_4x4x1_16b_f32 v[124:127], v16, v16, 0
	s_nop 0
	v_mfma_f32_4x4x1_16b_f32 v[108:111], v16, v16, 0
	s_nop 0
	v_mfma_f32_4x4x1_16b_f32 v[116:119], v16, v16, 0
	s_nop 0
	v_mfma_f32_4x4x1_16b_f32 v[84:87], v16, v16, 0
	s_nop 0
	v_mfma_f32_4x4x1_16b_f32 v[96:99], v16, v16, 0
	s_nop 0
	v_mfma_f32_4x4x1_16b_f32 v[64:67], v16, v16, 0
	s_nop 0
	v_mfma_f32_4x4x1_16b_f32 v[72:75], v16, v16, 0
	s_nop 0
	v_mfma_f32_4x4x1_16b_f32 v[48:51], v16, v16, 0
	s_nop 0
	v_mfma_f32_4x4x1_16b_f32 v[60:63], v16, v16, 0
	s_nop 0
	v_mfma_f32_4x4x1_16b_f32 v[28:31], v16, v16, 0
	s_nop 0
	v_mfma_f32_4x4x1_16b_f32 v[36:39], v16, v16, 0
	s_nop 0
	v_mfma_f32_4x4x1_16b_f32 v[8:11], v16, v16, 0
	s_nop 0
	v_mfma_f32_4x4x1_16b_f32 v[12:15], v16, v16, 0
	s_nop 0
	v_mfma_f32_4x4x1_16b_f32 v[0:3], v16, v16, 0
	s_nop 0
	v_mfma_f32_4x4x1_16b_f32 v[4:7], v16, v16, 0
	s_nop 0
	v_mfma_f32_4x4x1_16b_f32 v[92:95], v16, v16, 0
	s_nop 0
	v_mfma_f32_4x4x1_16b_f32 v[100:103], v16, v16, 0
	s_nop 0
	v_mfma_f32_4x4x1_16b_f32 v[68:71], v16, v16, 0
	s_nop 0
	v_mfma_f32_4x4x1_16b_f32 v[76:79], v16, v16, 0
	s_nop 0
	v_mfma_f32_4x4x1_16b_f32 v[44:47], v16, v16, 0
	s_nop 0
	v_mfma_f32_4x4x1_16b_f32 v[56:59], v16, v16, 0
	s_nop 0
	v_mfma_f32_4x4x1_16b_f32 v[24:27], v16, v16, 0
	s_nop 0
	v_mfma_f32_4x4x1_16b_f32 v[16:19], v16, v16, 0
	s_cbranch_vccnz .LBB0_199
	s_barrier
	s_branch .LBB0_199
.LBB0_210:
	s_waitcnt vmcnt(0)
	s_barrier
.LBB0_211:
	s_cmp_eq_u32 s100, 1
	s_cbranch_scc0 .Lqs9_skip

.Lqs9_own:
	s_cmp_eq_u32 s99, 0
	s_cbranch_scc0 .Lqs9_done
	s_and_b32 s0, s98, 15
	s_cmp_eq_u32 s0, 0
	s_cbranch_scc1 .Lqs9_done
	v_subrev_u32_e32 v0, 0x100, v0
	s_mov_b32 s1, 0

.Lqs9_wait:
	s_barrier
	s_mov_b64 s[2:3], -1
	s_branch .LBB0_267
.Lqs9_skip:
	s_cmp_gt_i32 s91, 2
	s_cselect_b64 s[2:3], -1, 0
	s_and_b64 s[0:1], s[4:5], s[2:3]
	s_andn2_b64 vcc, exec, s[0:1]
	s_cbranch_vccnz .LBB0_267
	s_cmp_gt_u32 s80, 63
	s_waitcnt lgkmcnt(0)
	s_mov_b64 s[8:9], 0
	s_cbranch_scc1 .LBB0_214
	v_mbcnt_hi_u32_b32 v0, -1, v217
	v_cmp_eq_u32_e32 vcc, 0, v0
	s_and_b64 s[8:9], vcc, exec

.LBB0_267:
	s_cmp_eq_u32 s100, 1
	s_cbranch_scc0 .Lqo_p2a
	s_lshl_b32 s6, s98, 2
	s_add_i32 s6, s6, s99
	s_lshr_b32 s0, s98, 4
	s_lshl_b32 s0, s0, 9
	s_lshl_b32 s1, s99, 3
	s_add_i32 s1, s1, s88
	s_lshl_b32 s1, s1, 4
	s_add_i32 s36, s0, s1
	s_and_b32 s0, s98, 15
	s_add_i32 s36, s36, s0

.LBB0_271:
	s_ashr_i32 s27, s26, 31
	s_lshr_b32 s28, s27, 26
	s_add_i32 s29, s26, s28
	s_ashr_i32 s28, s29, 6
	s_andn2_b32 s29, s29, 63
	s_sub_i32 s41, s26, s29
	s_lshl_b32 s30, s41, 7
	s_ashr_i32 s29, s28, 31
	s_lshl_b64 s[42:43], s[28:29], 13
	s_ashr_i32 s31, s30, 31
	s_add_u32 s40, s42, s30
	s_addc_u32 s39, s43, s31
	s_cmp_lt_i32 s41, 1
	s_mul_i32 s42, s40, 0xc00
	s_cbranch_scc1 .LBB0_273
	s_mul_i32 s43, s39, 0xc00
	s_mul_hi_u32 s44, s40, 0xc00
	s_add_i32 s43, s44, s43
	s_add_u32 s44, s8, s42
	s_addc_u32 s45, s13, s43
	s_cmp_eq_u32 s100, 1
	s_cbranch_scc0 .Lqo_h2a
	s_cmp_eq_u32 s99, 0
	s_cbranch_scc0 .Lqo_h2a
	s_mul_i32 s54, s98, 9216
	s_add_u32 s54, s54, 0xe002400
	s_add_u32 s44, s8, s54
	s_addc_u32 s45, s13, 0
.Lqo_h2a:
	v_lshl_add_u64 v[64:65], v[102:103], 1, s[44:45]
	v_add_co_u32_e32 v66, vcc, 0xffffe000, v64
	s_nop 1
	v_addc_co_u32_e32 v67, vcc, -1, v65, vcc
	v_add_co_u32_e32 v68, vcc, 0xfffff000, v64
	s_nop 1
	v_addc_co_u32_e32 v69, vcc, -1, v65, vcc
	global_load_ushort v66, v[66:67], off sc1
	s_nop 0
	global_load_ushort v67, v[68:69], off offset:-1024 sc1
	s_nop 0
	global_load_ushort v64, v[64:65], off offset:-2048 sc1
	s_waitcnt vmcnt(2)
	v_lshlrev_b32_e32 v134, 16, v66
	s_waitcnt vmcnt(1)
	v_lshlrev_b32_e32 v135, 16, v67
	s_waitcnt vmcnt(0)
	v_lshlrev_b32_e32 v69, 16, v64
	s_branch .LBB0_274

.LBB0_290:
	s_ashr_i32 s5, s4, 31
	s_lshr_b32 s20, s5, 26
	s_add_i32 s21, s4, s20
	s_ashr_i32 s20, s21, 6
	s_andn2_b32 s21, s21, 63
	s_sub_i32 s31, s4, s21
	s_lshl_b32 s24, s31, 7
	s_ashr_i32 s21, s20, 31
	s_lshl_b64 s[40:41], s[20:21], 13
	s_ashr_i32 s25, s24, 31
	s_add_u32 s30, s40, s24
	s_addc_u32 s29, s41, s25
	s_cmp_lt_i32 s31, 1
	s_mul_i32 s33, s30, 0xc00
	s_cbranch_scc1 .LBB0_292
	s_mul_i32 s35, s29, 0xc00
	s_mul_hi_u32 s37, s30, 0xc00
	s_add_i32 s37, s37, s35
	s_add_u32 s40, s8, s33
	s_addc_u32 s41, s26, s37
	s_cmp_eq_u32 s100, 1
	s_cbranch_scc0 .Lqo_h2b
	s_cmp_eq_u32 s99, 0
	s_cbranch_scc0 .Lqo_h2b
	s_mul_i32 s54, s98, 9216
	s_add_u32 s54, s54, 0xe002400
	s_add_u32 s40, s8, s54
	s_addc_u32 s41, s26, 0
.Lqo_h2b:
	v_lshl_add_u64 v[64:65], v[102:103], 1, s[40:41]
	v_add_co_u32_e32 v66, vcc, 0xffffe000, v64
	s_nop 1
	v_addc_co_u32_e32 v67, vcc, -1, v65, vcc
	v_add_co_u32_e32 v68, vcc, 0xfffff000, v64
	s_nop 1
	v_addc_co_u32_e32 v69, vcc, -1, v65, vcc
	global_load_ushort v70, v[66:67], off sc1
	global_load_ushort v71, v[68:69], off offset:-1024 sc1
	global_load_ushort v72, v[64:65], off offset:-2048 sc1
	s_waitcnt vmcnt(2)
	v_lshlrev_b32_e32 v136, 16, v70
	s_waitcnt vmcnt(1)
	v_lshlrev_b32_e32 v137, 16, v71
	s_waitcnt vmcnt(0)
	v_lshlrev_b32_e32 v69, 16, v72
	s_branch .LBB0_293

.LBB0_297:
	s_cmp_eq_u32 s100, 1
	s_cbranch_scc0 .Lqo_p2ar
	s_and_b32 s0, s79, 31
	s_lshl_b32 s0, s0, 3
	s_lshr_b32 s1, s79, 5
	s_add_i32 s6, s0, s1
	s_lshl_b32 s0, s79, 3
	s_add_i32 s36, s0, s88

	.amdhsa_kernel _Z9hymba_fwd4Args
		.amdhsa_group_segment_fixed_size 0
		.amdhsa_private_segment_fixed_size 0
		.amdhsa_kernarg_size 560
		.amdhsa_user_sgpr_count 2
		.amdhsa_user_sgpr_dispatch_ptr 0
		.amdhsa_user_sgpr_queue_ptr 0
		.amdhsa_user_sgpr_kernarg_segment_ptr 1
		.amdhsa_user_sgpr_dispatch_id 0
		.amdhsa_user_sgpr_kernarg_preload_length 0
		.amdhsa_user_sgpr_kernarg_preload_offset 0
		.amdhsa_user_sgpr_private_segment_size 0
		.amdhsa_uses_dynamic_stack 0
		.amdhsa_enable_private_segment 0
		.amdhsa_system_sgpr_workgroup_id_x 1
		.amdhsa_system_sgpr_workgroup_id_y 0
		.amdhsa_system_sgpr_workgroup_id_z 0
		.amdhsa_system_sgpr_workgroup_info 0
		.amdhsa_system_vgpr_workitem_id 0
		.amdhsa_next_free_vgpr 256
		.amdhsa_next_free_sgpr 102
		.amdhsa_accum_offset 256
		.amdhsa_reserve_vcc 1
		.amdhsa_float_round_mode_32 0
		.amdhsa_float_round_mode_16_64 0
		.amdhsa_float_denorm_mode_32 3
		.amdhsa_float_denorm_mode_16_64 3
		.amdhsa_dx10_clamp 1
		.amdhsa_ieee_mode 1
		.amdhsa_fp16_overflow 0
		.amdhsa_tg_split 0
		.amdhsa_exception_fp_ieee_invalid_op 0
		.amdhsa_exception_fp_denorm_src 0
		.amdhsa_exception_fp_ieee_div_zero 0
		.amdhsa_exception_fp_ieee_overflow 0
		.amdhsa_exception_fp_ieee_underflow 0
		.amdhsa_exception_fp_ieee_inexact 0
		.amdhsa_exception_int_div_zero 0
	.end_amdhsa_kernel

amdhsa.kernels:
  - .agpr_count:     0
    .args:
      - .offset:         0
        .size:           304
        .value_kind:     by_value
      - .offset:         304
        .size:           4
        .value_kind:     hidden_block_count_x
      - .offset:         308
        .size:           4
        .value_kind:     hidden_block_count_y
      - .offset:         312
        .size:           4
        .value_kind:     hidden_block_count_z
      - .offset:         316
        .size:           2
        .value_kind:     hidden_group_size_x
      - .offset:         318
        .size:           2
        .value_kind:     hidden_group_size_y
      - .offset:         320
        .size:           2
        .value_kind:     hidden_group_size_z
      - .offset:         322
        .size:           2
        .value_kind:     hidden_remainder_x
      - .offset:         324
        .size:           2
        .value_kind:     hidden_remainder_y
      - .offset:         326
        .size:           2
        .value_kind:     hidden_remainder_z
      - .offset:         344
        .size:           8
        .value_kind:     hidden_global_offset_x
      - .offset:         352
        .size:           8
        .value_kind:     hidden_global_offset_y
      - .offset:         360
        .size:           8
        .value_kind:     hidden_global_offset_z
      - .offset:         368
        .size:           2
        .value_kind:     hidden_grid_dims
      - .offset:         424
        .size:           4
        .value_kind:     hidden_dynamic_lds_size
    .group_segment_fixed_size: 0
    .kernarg_segment_align: 8
    .kernarg_segment_size: 560
    .language:       OpenCL C
    .language_version:
      - 2
      - 0
    .max_flat_workgroup_size: 512
    .name:           _Z9hymba_fwd4Args
    .private_segment_fixed_size: 0
    .sgpr_count:     108
    .sgpr_spill_count: 18
    .symbol:         _Z9hymba_fwd4Args.kd
    .uniform_work_group_size: 1
    .uses_dynamic_stack: false
    .vgpr_count:     256
    .vgpr_spill_count: 0
    .wavefront_size: 64
